# opt24: opt22 + grid barrier v2: all waiting workgroups poll the top-level arrival counter (threshold (gen+1)*nx) instead of the generation word; last leader's generation add removed
# speedup vs baseline: 1.0025x; 1.0025x over previous
.LBB0_152:
	v_readlane_b32 s4, v252, 20
	v_readlane_b32 s5, v252, 21
	v_cvt_f32_u32_e32 v1, v2
	v_sub_u32_e32 v4, 0, v2
	v_rcp_iflag_f32_e32 v1, v1
	s_nop 1
	global_atomic_add v3, v97, v197, s[4:5] sc0
	v_mul_f32_e32 v1, 0x4f7ffffe, v1
	v_cvt_u32_f32_e32 v1, v1
	v_mul_lo_u32 v4, v4, v1
	v_mul_hi_u32 v4, v1, v4
	v_add_u32_e32 v1, v1, v4
	s_waitcnt vmcnt(0)
	v_mul_hi_u32 v1, v3, v1
	v_mul_lo_u32 v4, v1, v2
	v_sub_u32_e32 v4, v3, v4
	v_add_u32_e32 v5, 1, v1
	v_cmp_ge_u32_e32 vcc, v4, v2
	v_add_u32_e32 v3, 1, v3
	s_nop 0
	v_cndmask_b32_e32 v1, v1, v5, vcc
	v_sub_u32_e32 v5, v4, v2
	v_cndmask_b32_e32 v4, v4, v5, vcc
	v_add_u32_e32 v5, 1, v1
	v_cmp_ge_u32_e32 vcc, v4, v2
	s_nop 1
	v_cndmask_b32_e32 v1, v1, v5, vcc
	v_mul_lo_u32 v4, v2, v1
	v_add_u32_e32 v2, v4, v2
	v_cmp_ne_u32_e32 vcc, v3, v2
	s_and_saveexec_b64 s[4:5], vcc
	s_xor_b64 s[4:5], exec, s[4:5]
	s_cbranch_execz .LBB0_166
	v_readlane_b32 s98, v251, 4
	v_add_u32_e32 v30, 1, v1
	v_mov_b32_e32 v31, s98
	ds_read_b32 v31, v31 offset:4
	s_waitcnt lgkmcnt(0)
	v_mul_lo_u32 v30, v30, v31
	v_readlane_b32 s6, v252, 24
	v_readlane_b32 s7, v252, 25
	s_waitcnt lgkmcnt(0)
	s_nop 3
	global_load_dword v0, v97, s[6:7] sc1
	s_waitcnt vmcnt(0)
	v_cmp_lt_u32_e32 vcc, v0, v30
	s_and_saveexec_b64 s[6:7], vcc
	s_cbranch_execz .LBB0_165
	s_mov_b32 s16, 1
	s_mov_b64 s[10:11], 0
	s_branch .LBB0_156

.LBB0_160:
	v_readlane_b32 s98, v251, 4
	v_add_u32_e32 v30, 1, v1
	v_mov_b32_e32 v31, s98
	ds_read_b32 v31, v31 offset:4
	s_waitcnt lgkmcnt(0)
	v_mul_lo_u32 v30, v30, v31
	v_readlane_b32 s14, v252, 24
	v_readlane_b32 s15, v252, 25
	s_add_i32 s16, s16, 1
	s_mov_b64 s[18:19], -1
	s_nop 2
	global_load_dword v0, v97, s[14:15] sc1
	s_waitcnt vmcnt(0)
	v_cmp_ge_u32_e32 vcc, v0, v30
	s_orn2_b64 s[14:15], vcc, exec
	s_branch .LBB0_155

.LBB0_169:
	s_or_b64 exec, exec, s[6:7]
	v_cvt_f32_u32_e32 v3, v0
	s_waitcnt vmcnt(0)
	v_readfirstlane_b32 s4, v2
	s_mov_b64 s[6:7], -1
	v_rcp_iflag_f32_e32 v3, v3
	v_add_u32_e32 v1, s4, v1
	v_add_u32_e32 v4, 1, v1
	v_readlane_b32 s4, v252, 26
	v_mul_f32_e32 v2, 0x4f7ffffe, v3
	v_cvt_u32_f32_e32 v2, v2
	v_sub_u32_e32 v3, 0, v0
	v_readlane_b32 s5, v252, 27
	v_mul_lo_u32 v3, v3, v2
	v_mul_hi_u32 v3, v2, v3
	v_add_u32_e32 v2, v2, v3
	v_mul_hi_u32 v2, v1, v2
	v_mul_lo_u32 v3, v2, v0
	v_sub_u32_e32 v1, v1, v3
	v_add_u32_e32 v5, 1, v2
	v_cmp_ge_u32_e32 vcc, v1, v0
	v_sub_u32_e32 v3, v1, v0
	s_nop 0
	v_cndmask_b32_e32 v2, v2, v5, vcc
	v_cndmask_b32_e32 v1, v1, v3, vcc
	v_add_u32_e32 v3, 1, v2
	v_cmp_ge_u32_e32 vcc, v1, v0
	s_nop 1
	v_cndmask_b32_e32 v2, v2, v3, vcc
	v_mul_lo_u32 v1, v0, v2
	v_add_u32_e32 v0, v1, v0
	v_cmp_ne_u32_e32 vcc, v4, v0
	v_mov_b64_e32 v[0:1], s[4:5]
	s_and_saveexec_b64 s[4:5], vcc
	s_cbranch_execz .LBB0_181
	v_readlane_b32 s98, v251, 4
	v_add_u32_e32 v30, 1, v2
	v_mov_b32_e32 v31, s98
	ds_read_b32 v31, v31 offset:4
	s_waitcnt lgkmcnt(0)
	v_mul_lo_u32 v30, v30, v31
	v_readlane_b32 s6, v252, 24
	v_readlane_b32 s7, v252, 25
	s_mov_b64 s[10:11], 0
	s_nop 3
	global_load_dword v0, v97, s[6:7] sc1
	s_waitcnt vmcnt(0)
	v_cmp_lt_u32_e32 vcc, v0, v30
	s_and_saveexec_b64 s[6:7], vcc
	s_cbranch_execz .LBB0_180
	s_mov_b32 s16, 1
	s_branch .LBB0_173

.LBB0_177:
	v_readlane_b32 s98, v251, 4
	v_add_u32_e32 v30, 1, v2
	v_mov_b32_e32 v31, s98
	ds_read_b32 v31, v31 offset:4
	s_waitcnt lgkmcnt(0)
	v_mul_lo_u32 v30, v30, v31
	v_readlane_b32 s14, v252, 24
	v_readlane_b32 s15, v252, 25
	s_add_i32 s16, s16, 1
	s_mov_b64 s[18:19], -1
	s_nop 2
	global_load_dword v0, v97, s[14:15] sc1
	s_waitcnt vmcnt(0)
	v_cmp_ge_u32_e32 vcc, v0, v30
	s_orn2_b64 s[14:15], vcc, exec
	s_branch .LBB0_172

.LBB0_181:
	s_or_b64 exec, exec, s[4:5]
	s_and_saveexec_b64 s[4:5], s[6:7]
	s_cbranch_execz .LBB0_183
.LBB0_183:
	s_or_b64 exec, exec, s[4:5]
	v_readlane_b32 s4, v252, 22
	v_readlane_b32 s5, v252, 23
	s_waitcnt vmcnt(0)
	buffer_inv sc1
	s_nop 2
	s_waitcnt vmcnt(0)

.LBB0_323:
	v_readlane_b32 s4, v252, 20
	v_readlane_b32 s5, v252, 21
	v_cvt_f32_u32_e32 v1, v2
	v_sub_u32_e32 v4, 0, v2
	v_rcp_iflag_f32_e32 v1, v1
	s_nop 1
	global_atomic_add v3, v97, v197, s[4:5] sc0
	v_mul_f32_e32 v1, 0x4f7ffffe, v1
	v_cvt_u32_f32_e32 v1, v1
	v_mul_lo_u32 v4, v4, v1
	v_mul_hi_u32 v4, v1, v4
	v_add_u32_e32 v1, v1, v4
	s_waitcnt vmcnt(0)
	v_mul_hi_u32 v1, v3, v1
	v_mul_lo_u32 v4, v1, v2
	v_sub_u32_e32 v4, v3, v4
	v_add_u32_e32 v5, 1, v1
	v_cmp_ge_u32_e32 vcc, v4, v2
	v_add_u32_e32 v3, 1, v3
	s_nop 0
	v_cndmask_b32_e32 v1, v1, v5, vcc
	v_sub_u32_e32 v5, v4, v2
	v_cndmask_b32_e32 v4, v4, v5, vcc
	v_add_u32_e32 v5, 1, v1
	v_cmp_ge_u32_e32 vcc, v4, v2
	s_nop 1
	v_cndmask_b32_e32 v1, v1, v5, vcc
	v_mul_lo_u32 v4, v2, v1
	v_add_u32_e32 v2, v4, v2
	v_cmp_ne_u32_e32 vcc, v3, v2
	s_and_saveexec_b64 s[4:5], vcc
	s_xor_b64 s[4:5], exec, s[4:5]
	s_cbranch_execz .LBB0_337
	v_readlane_b32 s98, v251, 4
	v_add_u32_e32 v30, 1, v1
	v_mov_b32_e32 v31, s98
	ds_read_b32 v31, v31 offset:4
	s_waitcnt lgkmcnt(0)
	v_mul_lo_u32 v30, v30, v31
	v_readlane_b32 s6, v252, 24
	v_readlane_b32 s7, v252, 25
	s_waitcnt lgkmcnt(0)
	s_nop 3
	global_load_dword v0, v97, s[6:7] sc1
	s_waitcnt vmcnt(0)
	v_cmp_lt_u32_e32 vcc, v0, v30
	s_and_saveexec_b64 s[6:7], vcc
	s_cbranch_execz .LBB0_336
	s_mov_b32 s24, 1
	s_mov_b64 s[12:13], 0
	s_branch .LBB0_327

.LBB0_331:
	v_readlane_b32 s98, v251, 4
	v_add_u32_e32 v30, 1, v1
	v_mov_b32_e32 v31, s98
	ds_read_b32 v31, v31 offset:4
	s_waitcnt lgkmcnt(0)
	v_mul_lo_u32 v30, v30, v31
	v_readlane_b32 s18, v252, 24
	v_readlane_b32 s19, v252, 25
	s_add_i32 s24, s24, 1
	s_mov_b64 s[20:21], -1
	s_nop 2
	global_load_dword v0, v97, s[18:19] sc1
	s_waitcnt vmcnt(0)
	v_cmp_ge_u32_e32 vcc, v0, v30
	s_orn2_b64 s[18:19], vcc, exec
	s_branch .LBB0_326

.LBB0_340:
	s_or_b64 exec, exec, s[6:7]
	s_waitcnt vmcnt(0)
	v_readfirstlane_b32 s4, v2
	v_cvt_f32_u32_e32 v2, v0
	v_sub_u32_e32 v3, 0, v0
	v_add_u32_e32 v1, s4, v1
	v_readlane_b32 s4, v252, 26
	v_rcp_iflag_f32_e32 v2, v2
	v_readlane_b32 s5, v252, 27
	s_mov_b64 s[6:7], -1
	v_mul_f32_e32 v2, 0x4f7ffffe, v2
	v_cvt_u32_f32_e32 v2, v2
	v_mul_lo_u32 v3, v3, v2
	v_mul_hi_u32 v3, v2, v3
	v_add_u32_e32 v2, v2, v3
	v_mul_hi_u32 v2, v1, v2
	v_mul_lo_u32 v3, v2, v0
	v_sub_u32_e32 v3, v1, v3
	v_cmp_ge_u32_e32 vcc, v3, v0
	v_add_u32_e32 v4, 1, v2
	v_add_u32_e32 v1, 1, v1
	v_cndmask_b32_e32 v2, v2, v4, vcc
	v_sub_u32_e32 v4, v3, v0
	v_cndmask_b32_e32 v3, v3, v4, vcc
	v_cmp_ge_u32_e32 vcc, v3, v0
	v_add_u32_e32 v3, 1, v2
	s_nop 0
	v_cndmask_b32_e32 v2, v2, v3, vcc
	v_mul_lo_u32 v3, v0, v2
	v_add_u32_e32 v0, v3, v0
	v_cmp_ne_u32_e32 vcc, v1, v0
	v_mov_b64_e32 v[0:1], s[4:5]
	s_and_saveexec_b64 s[4:5], vcc
	s_cbranch_execz .LBB0_352
	v_readlane_b32 s98, v251, 4
	v_add_u32_e32 v30, 1, v2
	v_mov_b32_e32 v31, s98
	ds_read_b32 v31, v31 offset:4
	s_waitcnt lgkmcnt(0)
	v_mul_lo_u32 v30, v30, v31
	v_readlane_b32 s6, v252, 24
	v_readlane_b32 s7, v252, 25
	s_mov_b64 s[12:13], 0
	s_nop 3
	global_load_dword v0, v97, s[6:7] sc1
	s_waitcnt vmcnt(0)
	v_cmp_lt_u32_e32 vcc, v0, v30
	s_and_saveexec_b64 s[6:7], vcc
	s_cbranch_execz .LBB0_351
	s_mov_b32 s24, 1
	s_branch .LBB0_344

.LBB0_348:
	v_readlane_b32 s98, v251, 4
	v_add_u32_e32 v30, 1, v2
	v_mov_b32_e32 v31, s98
	ds_read_b32 v31, v31 offset:4
	s_waitcnt lgkmcnt(0)
	v_mul_lo_u32 v30, v30, v31
	v_readlane_b32 s18, v252, 24
	v_readlane_b32 s19, v252, 25
	s_add_i32 s24, s24, 1
	s_mov_b64 s[20:21], -1
	s_nop 2
	global_load_dword v0, v97, s[18:19] sc1
	s_waitcnt vmcnt(0)
	v_cmp_ge_u32_e32 vcc, v0, v30
	s_orn2_b64 s[18:19], vcc, exec
	s_branch .LBB0_343

.LBB0_352:
	s_or_b64 exec, exec, s[4:5]
	s_and_saveexec_b64 s[4:5], s[6:7]
	s_cbranch_execz .LBB0_354
.LBB0_354:
	s_or_b64 exec, exec, s[4:5]
	v_readlane_b32 s4, v252, 22
	v_readlane_b32 s5, v252, 23
	s_waitcnt vmcnt(0)
	buffer_inv sc1
	s_nop 2
	s_waitcnt vmcnt(0)

.LBB0_475:
	v_readlane_b32 s4, v252, 20
	v_readlane_b32 s5, v252, 21
	v_cvt_f32_u32_e32 v1, v2
	v_sub_u32_e32 v4, 0, v2
	v_rcp_iflag_f32_e32 v1, v1
	s_nop 1
	global_atomic_add v3, v97, v197, s[4:5] sc0
	v_mul_f32_e32 v1, 0x4f7ffffe, v1
	v_cvt_u32_f32_e32 v1, v1
	v_mul_lo_u32 v4, v4, v1
	v_mul_hi_u32 v4, v1, v4
	v_add_u32_e32 v1, v1, v4
	s_waitcnt vmcnt(0)
	v_mul_hi_u32 v1, v3, v1
	v_mul_lo_u32 v4, v1, v2
	v_sub_u32_e32 v4, v3, v4
	v_add_u32_e32 v5, 1, v1
	v_cmp_ge_u32_e32 vcc, v4, v2
	v_add_u32_e32 v3, 1, v3
	s_nop 0
	v_cndmask_b32_e32 v1, v1, v5, vcc
	v_sub_u32_e32 v5, v4, v2
	v_cndmask_b32_e32 v4, v4, v5, vcc
	v_add_u32_e32 v5, 1, v1
	v_cmp_ge_u32_e32 vcc, v4, v2
	s_nop 1
	v_cndmask_b32_e32 v1, v1, v5, vcc
	v_mul_lo_u32 v4, v2, v1
	v_add_u32_e32 v2, v4, v2
	v_cmp_ne_u32_e32 vcc, v3, v2
	s_and_saveexec_b64 s[4:5], vcc
	s_xor_b64 s[4:5], exec, s[4:5]
	s_cbranch_execz .LBB0_489
	v_readlane_b32 s98, v251, 4
	v_add_u32_e32 v30, 1, v1
	v_mov_b32_e32 v31, s98
	ds_read_b32 v31, v31 offset:4
	s_waitcnt lgkmcnt(0)
	v_mul_lo_u32 v30, v30, v31
	v_readlane_b32 s6, v252, 24
	v_readlane_b32 s7, v252, 25
	s_waitcnt lgkmcnt(0)
	s_nop 3
	global_load_dword v0, v97, s[6:7] sc1
	s_waitcnt vmcnt(0)
	v_cmp_lt_u32_e32 vcc, v0, v30
	s_and_saveexec_b64 s[6:7], vcc
	s_cbranch_execz .LBB0_488
	s_mov_b32 s16, 1
	s_mov_b64 s[12:13], 0
	s_branch .LBB0_479

.LBB0_483:
	v_readlane_b32 s98, v251, 4
	v_add_u32_e32 v30, 1, v1
	v_mov_b32_e32 v31, s98
	ds_read_b32 v31, v31 offset:4
	s_waitcnt lgkmcnt(0)
	v_mul_lo_u32 v30, v30, v31
	v_readlane_b32 s18, v252, 24
	v_readlane_b32 s19, v252, 25
	s_add_i32 s16, s16, 1
	s_mov_b64 s[20:21], -1
	s_nop 2
	global_load_dword v0, v97, s[18:19] sc1
	s_waitcnt vmcnt(0)
	v_cmp_ge_u32_e32 vcc, v0, v30
	s_orn2_b64 s[18:19], vcc, exec
	s_branch .LBB0_478

.LBB0_492:
	s_or_b64 exec, exec, s[6:7]
	s_waitcnt vmcnt(0)
	v_readfirstlane_b32 s4, v2
	v_cvt_f32_u32_e32 v2, v0
	v_sub_u32_e32 v3, 0, v0
	v_add_u32_e32 v1, s4, v1
	v_readlane_b32 s4, v252, 26
	v_rcp_iflag_f32_e32 v2, v2
	v_readlane_b32 s5, v252, 27
	s_mov_b64 s[6:7], -1
	v_mul_f32_e32 v2, 0x4f7ffffe, v2
	v_cvt_u32_f32_e32 v2, v2
	v_mul_lo_u32 v3, v3, v2
	v_mul_hi_u32 v3, v2, v3
	v_add_u32_e32 v2, v2, v3
	v_mul_hi_u32 v2, v1, v2
	v_mul_lo_u32 v3, v2, v0
	v_sub_u32_e32 v3, v1, v3
	v_cmp_ge_u32_e32 vcc, v3, v0
	v_add_u32_e32 v4, 1, v2
	v_add_u32_e32 v1, 1, v1
	v_cndmask_b32_e32 v2, v2, v4, vcc
	v_sub_u32_e32 v4, v3, v0
	v_cndmask_b32_e32 v3, v3, v4, vcc
	v_cmp_ge_u32_e32 vcc, v3, v0
	v_add_u32_e32 v3, 1, v2
	s_nop 0
	v_cndmask_b32_e32 v2, v2, v3, vcc
	v_mul_lo_u32 v3, v0, v2
	v_add_u32_e32 v0, v3, v0
	v_cmp_ne_u32_e32 vcc, v1, v0
	v_mov_b64_e32 v[0:1], s[4:5]
	s_and_saveexec_b64 s[4:5], vcc
	s_cbranch_execz .LBB0_504
	v_readlane_b32 s98, v251, 4
	v_add_u32_e32 v30, 1, v2
	v_mov_b32_e32 v31, s98
	ds_read_b32 v31, v31 offset:4
	s_waitcnt lgkmcnt(0)
	v_mul_lo_u32 v30, v30, v31
	v_readlane_b32 s6, v252, 24
	v_readlane_b32 s7, v252, 25
	s_mov_b64 s[12:13], 0
	s_nop 3
	global_load_dword v0, v97, s[6:7] sc1
	s_waitcnt vmcnt(0)
	v_cmp_lt_u32_e32 vcc, v0, v30
	s_and_saveexec_b64 s[6:7], vcc
	s_cbranch_execz .LBB0_503
	s_mov_b32 s16, 1
	s_branch .LBB0_496

.LBB0_500:
	v_readlane_b32 s98, v251, 4
	v_add_u32_e32 v30, 1, v2
	v_mov_b32_e32 v31, s98
	ds_read_b32 v31, v31 offset:4
	s_waitcnt lgkmcnt(0)
	v_mul_lo_u32 v30, v30, v31
	v_readlane_b32 s18, v252, 24
	v_readlane_b32 s19, v252, 25
	s_add_i32 s16, s16, 1
	s_mov_b64 s[20:21], -1
	s_nop 2
	global_load_dword v0, v97, s[18:19] sc1
	s_waitcnt vmcnt(0)
	v_cmp_ge_u32_e32 vcc, v0, v30
	s_orn2_b64 s[18:19], vcc, exec
	s_branch .LBB0_495

.LBB0_504:
	s_or_b64 exec, exec, s[4:5]
	s_and_saveexec_b64 s[4:5], s[6:7]
	s_cbranch_execz .LBB0_506
.LBB0_506:
	s_or_b64 exec, exec, s[4:5]
	v_readlane_b32 s4, v252, 22
	v_readlane_b32 s5, v252, 23
	s_waitcnt vmcnt(0)
	buffer_inv sc1
	s_nop 2
	s_waitcnt vmcnt(0)

.LBB0_767:
	s_or_b64 exec, exec, s[4:5]
	s_and_saveexec_b64 s[4:5], s[6:7]
	s_cbranch_execz .LBB0_769
.LBB0_769:
	s_or_b64 exec, exec, s[4:5]
	v_readlane_b32 s4, v252, 22
	v_readlane_b32 s5, v252, 23
	s_waitcnt vmcnt(0)
	buffer_inv sc1
	s_nop 2
	s_waitcnt vmcnt(0)

.LBB0_900:
	s_or_b64 exec, exec, s[4:5]
	s_and_saveexec_b64 s[4:5], s[6:7]
	s_cbranch_execz .LBB0_902
.LBB0_902:
	s_or_b64 exec, exec, s[4:5]
	v_readlane_b32 s4, v252, 22
	v_readlane_b32 s5, v252, 23
	s_waitcnt vmcnt(0)
	buffer_inv sc1
	s_nop 2
	s_waitcnt vmcnt(0)

.LBB0_961:
	s_or_b64 exec, exec, s[4:5]
	s_and_saveexec_b64 s[4:5], s[6:7]
	s_cbranch_execz .LBB0_963
.LBB0_963:
	s_or_b64 exec, exec, s[4:5]
	v_readlane_b32 s4, v252, 22
	v_readlane_b32 s5, v252, 23
	s_waitcnt vmcnt(0)
	buffer_inv sc1
	s_nop 2
	s_waitcnt vmcnt(0)

.LBB0_1135:
	s_or_b64 exec, exec, s[4:5]
	s_and_saveexec_b64 s[4:5], s[6:7]
	s_cbranch_execz .LBB0_1137
.LBB0_1137:
	s_or_b64 exec, exec, s[4:5]
	v_readlane_b32 s4, v252, 22
	v_readlane_b32 s5, v252, 23
	s_waitcnt vmcnt(0)
	buffer_inv sc1
	s_nop 2
	s_waitcnt vmcnt(0)

.LBB0_1193:
	v_readlane_b32 s4, v252, 20
	v_readlane_b32 s5, v252, 21
	v_cvt_f32_u32_e32 v1, v2
	v_sub_u32_e32 v4, 0, v2
	v_rcp_iflag_f32_e32 v1, v1
	s_nop 1
	global_atomic_add v3, v97, v197, s[4:5] sc0
	v_mul_f32_e32 v1, 0x4f7ffffe, v1
	v_cvt_u32_f32_e32 v1, v1
	v_mul_lo_u32 v4, v4, v1
	v_mul_hi_u32 v4, v1, v4
	v_add_u32_e32 v1, v1, v4
	s_waitcnt vmcnt(0)
	v_mul_hi_u32 v1, v3, v1
	v_mul_lo_u32 v4, v1, v2
	v_sub_u32_e32 v4, v3, v4
	v_add_u32_e32 v5, 1, v1
	v_cmp_ge_u32_e32 vcc, v4, v2
	v_add_u32_e32 v3, 1, v3
	s_nop 0
	v_cndmask_b32_e32 v1, v1, v5, vcc
	v_sub_u32_e32 v5, v4, v2
	v_cndmask_b32_e32 v4, v4, v5, vcc
	v_add_u32_e32 v5, 1, v1
	v_cmp_ge_u32_e32 vcc, v4, v2
	s_nop 1
	v_cndmask_b32_e32 v1, v1, v5, vcc
	v_mul_lo_u32 v4, v2, v1
	v_add_u32_e32 v2, v4, v2
	v_cmp_ne_u32_e32 vcc, v3, v2
	s_and_saveexec_b64 s[4:5], vcc
	s_xor_b64 s[4:5], exec, s[4:5]
	s_cbranch_execz .LBB0_1207
	v_readlane_b32 s98, v251, 4
	v_add_u32_e32 v30, 1, v1
	v_mov_b32_e32 v31, s98
	ds_read_b32 v31, v31 offset:4
	s_waitcnt lgkmcnt(0)
	v_mul_lo_u32 v30, v30, v31
	v_readlane_b32 s6, v252, 24
	v_readlane_b32 s7, v252, 25
	s_waitcnt lgkmcnt(0)
	s_nop 3
	global_load_dword v0, v97, s[6:7] sc1
	s_waitcnt vmcnt(0)
	v_cmp_lt_u32_e32 vcc, v0, v30
	s_and_saveexec_b64 s[6:7], vcc
	s_cbranch_execz .LBB0_1206
	s_mov_b32 s20, 1
	s_mov_b64 s[8:9], 0
	s_branch .LBB0_1197

.LBB0_1201:
	v_readlane_b32 s98, v251, 4
	v_add_u32_e32 v30, 1, v1
	v_mov_b32_e32 v31, s98
	ds_read_b32 v31, v31 offset:4
	s_waitcnt lgkmcnt(0)
	v_mul_lo_u32 v30, v30, v31
	v_readlane_b32 s12, v252, 24
	v_readlane_b32 s13, v252, 25
	s_add_i32 s20, s20, 1
	s_mov_b64 s[14:15], -1
	s_nop 2
	global_load_dword v0, v97, s[12:13] sc1
	s_waitcnt vmcnt(0)
	v_cmp_ge_u32_e32 vcc, v0, v30
	s_orn2_b64 s[12:13], vcc, exec
	s_branch .LBB0_1196

.LBB0_1210:
	s_or_b64 exec, exec, s[6:7]
	s_waitcnt vmcnt(0)
	v_readfirstlane_b32 s4, v2
	v_cvt_f32_u32_e32 v2, v0
	v_sub_u32_e32 v3, 0, v0
	v_add_u32_e32 v1, s4, v1
	v_readlane_b32 s4, v252, 26
	v_rcp_iflag_f32_e32 v2, v2
	v_readlane_b32 s5, v252, 27
	s_mov_b64 s[6:7], -1
	v_mul_f32_e32 v2, 0x4f7ffffe, v2
	v_cvt_u32_f32_e32 v2, v2
	v_mul_lo_u32 v3, v3, v2
	v_mul_hi_u32 v3, v2, v3
	v_add_u32_e32 v2, v2, v3
	v_mul_hi_u32 v2, v1, v2
	v_mul_lo_u32 v3, v2, v0
	v_sub_u32_e32 v3, v1, v3
	v_cmp_ge_u32_e32 vcc, v3, v0
	v_add_u32_e32 v4, 1, v2
	v_add_u32_e32 v1, 1, v1
	v_cndmask_b32_e32 v2, v2, v4, vcc
	v_sub_u32_e32 v4, v3, v0
	v_cndmask_b32_e32 v3, v3, v4, vcc
	v_cmp_ge_u32_e32 vcc, v3, v0
	v_add_u32_e32 v3, 1, v2
	s_nop 0
	v_cndmask_b32_e32 v2, v2, v3, vcc
	v_mul_lo_u32 v3, v0, v2
	v_add_u32_e32 v0, v3, v0
	v_cmp_ne_u32_e32 vcc, v1, v0
	v_mov_b64_e32 v[0:1], s[4:5]
	s_and_saveexec_b64 s[4:5], vcc
	s_cbranch_execz .LBB0_1222
	v_readlane_b32 s98, v251, 4
	v_add_u32_e32 v30, 1, v2
	v_mov_b32_e32 v31, s98
	ds_read_b32 v31, v31 offset:4
	s_waitcnt lgkmcnt(0)
	v_mul_lo_u32 v30, v30, v31
	v_readlane_b32 s6, v252, 24
	v_readlane_b32 s7, v252, 25
	s_mov_b64 s[8:9], 0
	s_nop 3
	global_load_dword v0, v97, s[6:7] sc1
	s_waitcnt vmcnt(0)
	v_cmp_lt_u32_e32 vcc, v0, v30
	s_and_saveexec_b64 s[6:7], vcc
	s_cbranch_execz .LBB0_1221
	s_mov_b32 s20, 1
	s_branch .LBB0_1214

.LBB0_1218:
	v_readlane_b32 s98, v251, 4
	v_add_u32_e32 v30, 1, v2
	v_mov_b32_e32 v31, s98
	ds_read_b32 v31, v31 offset:4
	s_waitcnt lgkmcnt(0)
	v_mul_lo_u32 v30, v30, v31
	v_readlane_b32 s12, v252, 24
	v_readlane_b32 s13, v252, 25
	s_add_i32 s20, s20, 1
	s_mov_b64 s[14:15], -1
	s_nop 2
	global_load_dword v0, v97, s[12:13] sc1
	s_waitcnt vmcnt(0)
	v_cmp_ge_u32_e32 vcc, v0, v30
	s_orn2_b64 s[12:13], vcc, exec
	s_branch .LBB0_1213

.LBB0_1222:
	s_or_b64 exec, exec, s[4:5]
	s_and_saveexec_b64 s[4:5], s[6:7]
	s_cbranch_execz .LBB0_1224
.LBB0_1224:
	s_or_b64 exec, exec, s[4:5]
	v_readlane_b32 s4, v252, 22
	v_readlane_b32 s5, v252, 23
	s_waitcnt vmcnt(0)
	buffer_inv sc1
	s_nop 2
	s_waitcnt vmcnt(0)

.LBB0_1299:
	s_or_b64 exec, exec, s[4:5]
	s_and_saveexec_b64 s[4:5], s[6:7]
	s_cbranch_execz .LBB0_1301
.LBB0_1301:
	s_or_b64 exec, exec, s[4:5]
	v_readlane_b32 s4, v252, 22
	v_readlane_b32 s5, v252, 23
	s_waitcnt vmcnt(0)
	buffer_inv sc1
	s_nop 2
	s_waitcnt vmcnt(0)

.LBB0_1479:
	v_readlane_b32 s4, v252, 20
	v_readlane_b32 s5, v252, 21
	v_cvt_f32_u32_e32 v1, v2
	v_sub_u32_e32 v4, 0, v2
	v_rcp_iflag_f32_e32 v1, v1
	s_nop 1
	global_atomic_add v3, v97, v197, s[4:5] sc0
	v_mul_f32_e32 v1, 0x4f7ffffe, v1
	v_cvt_u32_f32_e32 v1, v1
	v_mul_lo_u32 v4, v4, v1
	v_mul_hi_u32 v4, v1, v4
	v_add_u32_e32 v1, v1, v4
	s_waitcnt vmcnt(0)
	v_mul_hi_u32 v1, v3, v1
	v_mul_lo_u32 v4, v1, v2
	v_sub_u32_e32 v4, v3, v4
	v_add_u32_e32 v5, 1, v1
	v_cmp_ge_u32_e32 vcc, v4, v2
	v_add_u32_e32 v3, 1, v3
	s_nop 0
	v_cndmask_b32_e32 v1, v1, v5, vcc
	v_sub_u32_e32 v5, v4, v2
	v_cndmask_b32_e32 v4, v4, v5, vcc
	v_add_u32_e32 v5, 1, v1
	v_cmp_ge_u32_e32 vcc, v4, v2
	s_nop 1
	v_cndmask_b32_e32 v1, v1, v5, vcc
	v_mul_lo_u32 v4, v2, v1
	v_add_u32_e32 v2, v4, v2
	v_cmp_ne_u32_e32 vcc, v3, v2
	s_and_saveexec_b64 s[4:5], vcc
	s_xor_b64 s[4:5], exec, s[4:5]
	s_cbranch_execz .LBB0_1493
	v_readlane_b32 s98, v251, 4
	v_add_u32_e32 v30, 1, v1
	v_mov_b32_e32 v31, s98
	ds_read_b32 v31, v31 offset:4
	s_waitcnt lgkmcnt(0)
	v_mul_lo_u32 v30, v30, v31
	v_readlane_b32 s6, v252, 24
	v_readlane_b32 s7, v252, 25
	s_waitcnt lgkmcnt(0)
	s_nop 3
	global_load_dword v0, v97, s[6:7] sc1
	s_waitcnt vmcnt(0)
	v_cmp_lt_u32_e32 vcc, v0, v30
	s_and_saveexec_b64 s[6:7], vcc
	s_cbranch_execz .LBB0_1492
	s_mov_b32 s16, 1
	s_mov_b64 s[8:9], 0
	s_branch .LBB0_1483

.LBB0_1487:
	v_readlane_b32 s98, v251, 4
	v_add_u32_e32 v30, 1, v1
	v_mov_b32_e32 v31, s98
	ds_read_b32 v31, v31 offset:4
	s_waitcnt lgkmcnt(0)
	v_mul_lo_u32 v30, v30, v31
	v_readlane_b32 s12, v252, 24
	v_readlane_b32 s13, v252, 25
	s_add_i32 s16, s16, 1
	s_mov_b64 s[14:15], -1
	s_nop 2
	global_load_dword v0, v97, s[12:13] sc1
	s_waitcnt vmcnt(0)
	v_cmp_ge_u32_e32 vcc, v0, v30
	s_orn2_b64 s[12:13], vcc, exec
	s_branch .LBB0_1482

.LBB0_1496:
	s_or_b64 exec, exec, s[6:7]
	s_waitcnt vmcnt(0)
	v_readfirstlane_b32 s4, v2
	v_cvt_f32_u32_e32 v2, v0
	v_sub_u32_e32 v3, 0, v0
	v_add_u32_e32 v1, s4, v1
	v_readlane_b32 s4, v252, 26
	v_rcp_iflag_f32_e32 v2, v2
	v_readlane_b32 s5, v252, 27
	s_mov_b64 s[6:7], -1
	v_mul_f32_e32 v2, 0x4f7ffffe, v2
	v_cvt_u32_f32_e32 v2, v2
	v_mul_lo_u32 v3, v3, v2
	v_mul_hi_u32 v3, v2, v3
	v_add_u32_e32 v2, v2, v3
	v_mul_hi_u32 v2, v1, v2
	v_mul_lo_u32 v3, v2, v0
	v_sub_u32_e32 v3, v1, v3
	v_cmp_ge_u32_e32 vcc, v3, v0
	v_add_u32_e32 v4, 1, v2
	v_add_u32_e32 v1, 1, v1
	v_cndmask_b32_e32 v2, v2, v4, vcc
	v_sub_u32_e32 v4, v3, v0
	v_cndmask_b32_e32 v3, v3, v4, vcc
	v_cmp_ge_u32_e32 vcc, v3, v0
	v_add_u32_e32 v3, 1, v2
	s_nop 0
	v_cndmask_b32_e32 v2, v2, v3, vcc
	v_mul_lo_u32 v3, v0, v2
	v_add_u32_e32 v0, v3, v0
	v_cmp_ne_u32_e32 vcc, v1, v0
	v_mov_b64_e32 v[0:1], s[4:5]
	s_and_saveexec_b64 s[4:5], vcc
	s_cbranch_execz .LBB0_1508
	v_readlane_b32 s98, v251, 4
	v_add_u32_e32 v30, 1, v2
	v_mov_b32_e32 v31, s98
	ds_read_b32 v31, v31 offset:4
	s_waitcnt lgkmcnt(0)
	v_mul_lo_u32 v30, v30, v31
	v_readlane_b32 s6, v252, 24
	v_readlane_b32 s7, v252, 25
	s_mov_b64 s[8:9], 0
	s_nop 3
	global_load_dword v0, v97, s[6:7] sc1
	s_waitcnt vmcnt(0)
	v_cmp_lt_u32_e32 vcc, v0, v30
	s_and_saveexec_b64 s[6:7], vcc
	s_cbranch_execz .LBB0_1507
	s_mov_b32 s16, 1
	s_branch .LBB0_1500

.LBB0_1504:
	v_readlane_b32 s98, v251, 4
	v_add_u32_e32 v30, 1, v2
	v_mov_b32_e32 v31, s98
	ds_read_b32 v31, v31 offset:4
	s_waitcnt lgkmcnt(0)
	v_mul_lo_u32 v30, v30, v31
	v_readlane_b32 s12, v252, 24
	v_readlane_b32 s13, v252, 25
	s_add_i32 s16, s16, 1
	s_mov_b64 s[14:15], -1
	s_nop 2
	global_load_dword v0, v97, s[12:13] sc1
	s_waitcnt vmcnt(0)
	v_cmp_ge_u32_e32 vcc, v0, v30
	s_orn2_b64 s[12:13], vcc, exec
	s_branch .LBB0_1499

.LBB0_1508:
	s_or_b64 exec, exec, s[4:5]
	s_and_saveexec_b64 s[4:5], s[6:7]
	s_cbranch_execz .LBB0_1510
.LBB0_1510:
	s_or_b64 exec, exec, s[4:5]
	v_readlane_b32 s4, v252, 22
	v_readlane_b32 s5, v252, 23
	s_waitcnt vmcnt(0)
	buffer_inv sc1
	s_nop 2
	s_waitcnt vmcnt(0)

.LBB0_1588:
	s_or_b64 exec, exec, s[4:5]
	s_and_saveexec_b64 s[4:5], s[6:7]
	s_cbranch_execz .LBB0_1590
.LBB0_1590:
	s_or_b64 exec, exec, s[4:5]
	v_readlane_b32 s4, v252, 22
	v_readlane_b32 s5, v252, 23
	s_waitcnt vmcnt(0)
	buffer_inv sc1
	s_nop 2
	s_waitcnt vmcnt(0)

.LBB0_1665:
	s_or_b64 exec, exec, s[4:5]
	s_and_saveexec_b64 s[4:5], s[6:7]
	s_cbranch_execz .LBB0_1667
.LBB0_1667:
	s_or_b64 exec, exec, s[4:5]
	v_readlane_b32 s4, v252, 22
	v_readlane_b32 s5, v252, 23
	s_waitcnt vmcnt(0)
	buffer_inv sc1
	s_nop 2
	s_waitcnt vmcnt(0)

.LBB0_1760:
	s_getpc_b64 s[98:99]
